# attention latent loop: row-sum halves combined once per unit instead of per tile; row-max halves combined only in the rare re-reference path (threshold test runs on per-lane partial max); reference==0
# speedup vs baseline: 1.0079x; 1.0033x over previous
.LBB0_783:
	s_and_b64 vcc, exec, s[0:1]
	s_cbranch_vccz .LBB0_762
	s_ashr_i32 s0, s16, 7
	s_lshl_b32 s18, s0, 11
	s_and_b32 s1, s17, 0x780
	s_or_b32 s17, s18, s1
	s_lshl_b32 s1, s16, 3
	s_and_b32 s1, s1, 0x380
	v_mbcnt_lo_u32_b32 v171, -1, 0
	v_mbcnt_hi_u32_b32 v171, -1, v171
	s_lshl_b32 s96, s1, 1
	v_lshlrev_b32_e32 v20, 3, v171
	v_and_b32_e32 v0, 0x78, v20
	s_add_u32 s20, s6, s96
	v_lshlrev_b32_e32 v16, 1, v0
	s_addc_u32 s21, s7, 0
	v_mov_b32_e32 v17, v113
	v_add_u32_e32 v172, s4, v171
	v_lshl_add_u64 v[166:167], s[20:21], 0, v[16:17]
	s_add_u32 s20, s8, s96
	v_ashrrev_i32_e32 v181, 4, v172
	s_addc_u32 s21, s9, 0
	v_lshl_add_u64 v[168:169], s[20:21], 0, v[16:17]
	v_mad_u32_u24 v241, v181, s62, v16
	v_add_u32_e32 v34, s18, v181
	v_mad_i64_i32 v[0:1], s[20:21], v34, s62, v[168:169]
	v_add_co_u32_e32 v4, vcc, s74, v0
	v_mad_i64_i32 v[8:9], s[20:21], v34, s62, v[166:167]
	s_nop 0
	v_addc_co_u32_e32 v5, vcc, 0, v1, vcc
	v_add_co_u32_e32 v12, vcc, s74, v8
	global_load_dwordx4 v[0:3], v[0:1], off
	s_nop 0
	global_load_dwordx4 v[4:7], v[4:5], off
	v_addc_co_u32_e32 v13, vcc, 0, v9, vcc
	global_load_dwordx4 v[8:11], v[8:9], off
	s_nop 0
	global_load_dwordx4 v[12:15], v[12:13], off
	v_lshrrev_b32_e32 v17, 1, v172
	v_and_b32_e32 v173, 31, v171
	v_and_b32_e32 v176, 0x60, v17
	v_mov_b64_e32 v[18:19], s[50:51]
	v_ashrrev_i32_e32 v175, 8, v172
	v_or3_b32 v29, v173, s17, v176
	v_bfe_u32 v22, v20, 5, 2
	v_lshlrev_b32_e32 v20, 6, v175
	v_mad_i64_i32 v[18:19], s[20:21], v29, s62, v[18:19]
	v_bfe_u32 v174, v171, 5, 1
	v_ashrrev_i32_e32 v21, 31, v20
	v_lshl_add_u64 v[18:19], v[18:19], 0, s[96:97]
	v_lshlrev_b32_e32 v112, 4, v174
	v_lshl_add_u64 v[18:19], v[20:21], 1, v[18:19]
	v_lshl_add_u64 v[18:19], v[18:19], 0, v[112:113]
	global_load_dwordx4 v[122:125], v[18:19], off
	global_load_dwordx4 v[126:129], v[18:19], off offset:32
	global_load_dwordx4 v[118:121], v[18:19], off offset:64
	global_load_dwordx4 v[114:117], v[18:19], off offset:96
	v_and_b32_e32 v17, 0xfffff0, v181
	v_lshlrev_b32_e32 v24, 1, v181
	v_add_u32_e32 v27, 32, v181
	v_lshrrev_b32_e32 v25, 1, v181
	v_and_b32_e32 v26, 3, v181
	v_and_or_b32 v17, v181, 8, v17
	v_and_b32_e32 v20, 0xfffff0, v27
	v_lshlrev_b32_e32 v21, 1, v27
	v_and_b32_e32 v23, 0x70, v172
	v_lshlrev_b32_e32 v28, 8, v181
	v_and_or_b32 v24, v181, 4, v26
	v_lshlrev_b32_e32 v26, 8, v27
	v_lshrrev_b32_e32 v17, 1, v17
	v_and_or_b32 v20, v27, 8, v20
	v_and_b32_e32 v25, 48, v16
	v_bitop3_b32 v182, v16, v28, v23 bitop3:0xde
	v_bitop3_b32 v183, v26, v16, v23 bitop3:0xf6
	v_and_b32_e32 v243, 16, v181
	v_lshlrev_b32_e32 v243, 3, v243
	v_xor_b32_e32 v182, v243, v182
	v_xor_b32_e32 v183, v243, v183
	v_or_b32_e32 v16, v17, v22
	v_lshrrev_b32_e32 v17, 1, v20
	v_lshlrev_b32_e32 v24, 6, v24
	v_lshlrev_b32_e32 v16, 9, v16
	v_or_b32_e32 v17, v17, v22
	v_or3_b32 v184, v16, v24, v25
	v_lshlrev_b32_e32 v16, 9, v17
	v_or3_b32 v185, v16, v24, v25
	v_add_u32_e32 v32, 0, v184
	v_add_u32_e32 v21, 0, v182
	v_add_u32_e32 v20, 0, v183
	v_add_u32_e32 v33, 0, v185
	s_waitcnt vmcnt(0)
	v_lshlrev_b32_e32 v38, 7, v175
	v_lshlrev_b32_e32 v189, 8, v173
	v_add_u32_e32 v191, 0, v189
	s_movk_i32 s1, 0x60
	s_waitcnt vmcnt(7)
	ds_write_b128 v32, v[0:3] offset:1024
	s_waitcnt vmcnt(6)
	ds_write_b128 v33, v[4:7] offset:1024
	s_waitcnt vmcnt(5)
	ds_write_b128 v21, v[8:11] offset:50176
	s_waitcnt vmcnt(4)
	ds_write_b128 v20, v[12:15] offset:50176
	v_add_u32_e32 v4, 64, v34
	v_mad_i64_i32 v[0:1], s[20:21], v4, s62, v[168:169]
	v_add_co_u32_e32 v2, vcc, s74, v0
	s_nop 1
	v_addc_co_u32_e32 v3, vcc, 0, v1, vcc
	global_load_dwordx4 v[16:19], v[0:1], off
	global_load_dwordx4 v[20:23], v[2:3], off
	v_mad_i64_i32 v[0:1], s[20:21], v4, s62, v[166:167]
	v_add_co_u32_e32 v2, vcc, s74, v0
	v_add_u32_e32 v4, 0x80, v34
	s_nop 0
	v_addc_co_u32_e32 v3, vcc, 0, v1, vcc
	global_load_dwordx4 v[24:27], v[0:1], off
	global_load_dwordx4 v[28:31], v[2:3], off
	v_mad_i64_i32 v[0:1], s[20:21], v4, s62, v[166:167]
	v_add_co_u32_e32 v2, vcc, s74, v0
	s_nop 1
	v_addc_co_u32_e32 v3, vcc, 0, v1, vcc
	global_load_dwordx4 v[142:145], v[2:3], off
	global_load_dwordx4 v[138:141], v[0:1], off
	v_mad_i64_i32 v[0:1], s[20:21], v4, s62, v[168:169]
	v_add_co_u32_e32 v2, vcc, s74, v0
	s_nop 1
	v_addc_co_u32_e32 v3, vcc, 0, v1, vcc
	global_load_dwordx4 v[134:137], v[2:3], off
	global_load_dwordx4 v[130:133], v[0:1], off
	v_lshlrev_b32_e32 v0, 4, v171
	v_and_b32_e32 v39, 0x70, v0
	v_bitop3_b32 v190, v38, v39, v112 bitop3:0x36
	v_and_b32_e32 v244, 16, v171
	v_lshlrev_b32_e32 v244, 3, v244
	v_xor_b32_e32 v190, v244, v190
	v_add_u32_e32 v34, v191, v190
	s_waitcnt lgkmcnt(0)
	s_barrier
	ds_read_b128 v[0:3], v34 offset:50176
	ds_read_b128 v[34:37], v34 offset:58368
	v_or_b32_e32 v38, v38, v112
	v_bitop3_b32 v188, v38, v39, 32 bitop3:0x36
	v_xor_b32_e32 v188, v244, v188
	v_add_u32_e32 v40, v191, v188
	s_waitcnt vmcnt(11) lgkmcnt(0)
	v_mfma_f32_32x32x16_bf16 v[64:79], v[34:37], v[122:125], 0
	ds_read_b128 v[34:37], v40 offset:50176
	v_bitop3_b32 v187, v38, v39, 64 bitop3:0x36
	v_bitop3_b32 v186, v38, v39, s1 bitop3:0x36
	v_xor_b32_e32 v187, v244, v187
	v_xor_b32_e32 v186, v244, v186
	v_add_u32_e32 v38, v191, v186
	v_mfma_f32_32x32x16_bf16 v[0:15], v[0:3], v[122:125], 0
	s_waitcnt vmcnt(10) lgkmcnt(0)
	v_mfma_f32_32x32x16_bf16 v[0:15], v[34:37], v[126:129], v[0:15]
	ds_read_b128 v[34:37], v40 offset:58368
	v_add_u32_e32 v40, v191, v187
	s_waitcnt lgkmcnt(0)
	v_mfma_f32_32x32x16_bf16 v[64:79], v[34:37], v[126:129], v[64:79]
	ds_read_b128 v[34:37], v40 offset:50176
	s_waitcnt vmcnt(9) lgkmcnt(0)
	v_mfma_f32_32x32x16_bf16 v[0:15], v[34:37], v[118:121], v[0:15]
	ds_read_b128 v[34:37], v40 offset:58368
	s_waitcnt lgkmcnt(0)
	v_mfma_f32_32x32x16_bf16 v[64:79], v[34:37], v[118:121], v[64:79]
	ds_read_b128 v[34:37], v38 offset:50176
	s_waitcnt vmcnt(8) lgkmcnt(0)
	v_mfma_f32_32x32x16_bf16 v[0:15], v[34:37], v[114:117], v[0:15]
	ds_read_b128 v[34:37], v38 offset:58368
	s_waitcnt lgkmcnt(0)
	v_mfma_f32_32x32x16_bf16 v[64:79], v[34:37], v[114:117], v[64:79]
	s_nop 8
	v_max_f32_e32 v34, v1, v1
	v_max_f32_e32 v35, v0, v0
	v_max_f32_e32 v34, v35, v34
	v_max3_f32 v34, v34, v2, v3
	v_max3_f32 v34, v34, v4, v5
	v_max3_f32 v34, v34, v6, v7
	v_max3_f32 v34, v34, v8, v9
	v_max3_f32 v34, v34, v10, v11
	v_max3_f32 v34, v34, v12, v13
	v_max3_f32 v34, v34, v14, v15
	v_max3_f32 v34, v34, v64, v65
	v_max3_f32 v34, v34, v66, v67
	v_max3_f32 v34, v34, v68, v69
	v_max3_f32 v34, v34, v70, v71
	v_max3_f32 v34, v34, v72, v73
	v_max3_f32 v34, v34, v74, v75
	v_max3_f32 v34, v34, v76, v77
	v_max3_f32 v34, v34, v78, v79
	v_mov_b32_e32 v35, v34
	s_nop 1
	v_permlane32_swap_b32_e32 v34, v35
	v_max_f32_e32 v35, v35, v35
	v_max_f32_e32 v34, v34, v34
	v_max_f32_e32 v34, v34, v35
	v_cmp_ge_f32_e32 vcc, s75, v34
	s_cmp_eq_u64 vcc, exec
	s_cbranch_scc0 .LBB0_814
	v_mov_b32_e32 v193, 1.0
	v_mov_b32_e32 v164, 0
	s_mov_b64 s[56:57], exec

.LBB0_787:
	s_mov_b32 s54, s0
	s_add_i32 s55, s28, -3
	s_lshl_b32 s21, s0, 14
	v_add_u32_e32 v180, s21, v191
	v_add_u32_e32 v84, v180, v190
	ds_read_b128 v[80:83], v84 offset:50176
	ds_read_b128 v[84:87], v84 offset:58368
	v_add_u32_e32 v195, v180, v188
	ds_read_b128 v[196:199], v195 offset:50176
	ds_read_b128 v[200:203], v195 offset:58368
	v_add_u32_e32 v195, v180, v187
	s_waitcnt lgkmcnt(3)
	v_mfma_f32_32x32x16_bf16 v[96:111], v[80:83], v[122:125], 0
	v_add_u32_e32 v180, v180, v186
	v_exp_f32_e32 v204, v72
	v_exp_f32_e32 v205, v73
	v_exp_f32_e32 v206, v74
	v_exp_f32_e32 v207, v75
	v_exp_f32_e32 v208, v76
	v_exp_f32_e32 v209, v77
	s_waitcnt lgkmcnt(2)
	v_mfma_f32_32x32x16_bf16 v[80:95], v[84:87], v[122:125], 0
	v_exp_f32_e32 v210, v78
	v_exp_f32_e32 v79, v79
	s_waitcnt lgkmcnt(1)
	v_mfma_f32_32x32x16_bf16 v[96:111], v[196:199], v[126:129], v[96:111]
	s_waitcnt lgkmcnt(0)
	v_mfma_f32_32x32x16_bf16 v[80:95], v[200:203], v[126:129], v[80:95]
	ds_read_b128 v[196:199], v195 offset:50176
	ds_read_b128 v[200:203], v195 offset:58368
	s_waitcnt lgkmcnt(1)
	v_mfma_f32_32x32x16_bf16 v[96:111], v[196:199], v[118:121], v[96:111]
	s_waitcnt lgkmcnt(0)
	v_mfma_f32_32x32x16_bf16 v[80:95], v[200:203], v[118:121], v[80:95]
	ds_read_b128 v[196:199], v180 offset:50176
	ds_read_b128 v[200:203], v180 offset:58368
	v_exp_f32_e32 v180, v64
	v_add_f32_e32 v64, v161, v159
	v_add_f32_e32 v195, v157, v160
	v_add_f32_e32 v64, v155, v64
	v_add_f32_e32 v195, v158, v195
	v_add_f32_e32 v64, v154, v64
	v_add_f32_e32 v195, v156, v195
	v_add_f32_e32 v64, v151, v64
	v_add_f32_e32 v195, v153, v195
	v_add_f32_e32 v64, v149, v64
	v_add_f32_e32 v195, v152, v195
	v_add_f32_e32 v64, v147, v64
	s_waitcnt lgkmcnt(1)
	v_mfma_f32_32x32x16_bf16 v[96:111], v[196:199], v[114:117], v[96:111]
	v_exp_f32_e32 v197, v65
	v_add_f32_e32 v195, v150, v195
	v_exp_f32_e32 v198, v66
	v_add_f32_e32 v64, v146, v64
	v_exp_f32_e32 v199, v67
	v_add_f32_e32 v195, v148, v195
	v_add_f32_e32 v64, v180, v64
	s_waitcnt lgkmcnt(0)
	v_mfma_f32_32x32x16_bf16 v[80:95], v[200:203], v[114:117], v[80:95]
	v_exp_f32_e32 v200, v68
	v_exp_f32_e32 v201, v69
	v_add_f32_e32 v195, v197, v195
	v_exp_f32_e32 v202, v70
	v_add_f32_e32 v64, v198, v64
	v_exp_f32_e32 v203, v71
	v_add_f32_e32 v195, v199, v195
	v_add_f32_e32 v64, v200, v64
	v_add_f32_e32 v195, v201, v195
	v_add_f32_e32 v64, v202, v64
	v_add_f32_e32 v195, v203, v195
	v_add_f32_e32 v64, v204, v64
	v_add_f32_e32 v195, v205, v195
	v_add_f32_e32 v64, v206, v64
	v_add_f32_e32 v195, v207, v195
	v_add_f32_e32 v64, v208, v64
	v_add_f32_e32 v195, v209, v195
	v_add_f32_e32 v64, v210, v64
	v_add_f32_e32 v195, v79, v195
	v_add_f32_e32 v195, v195, v64
	v_cvt_pk_bf16_f32 v64, v159, v161
	v_cvt_pk_bf16_f32 v65, v157, v160
	v_cvt_pk_bf16_f32 v66, v155, v158
	v_cvt_pk_bf16_f32 v67, v154, v156
	v_cvt_pk_bf16_f32 v68, v151, v153
	v_cvt_pk_bf16_f32 v69, v149, v152
	v_cvt_pk_bf16_f32 v70, v147, v150
	v_cvt_pk_bf16_f32 v71, v146, v148
	v_cvt_pk_bf16_f32 v72, v180, v197
	v_cvt_pk_bf16_f32 v73, v198, v199
	v_cvt_pk_bf16_f32 v74, v200, v201
	v_cvt_pk_bf16_f32 v75, v202, v203
	v_cvt_pk_bf16_f32 v76, v204, v205
	v_cvt_pk_bf16_f32 v77, v206, v207
	v_cvt_pk_bf16_f32 v78, v208, v209
	v_cvt_pk_bf16_f32 v79, v210, v79
	s_cmp_lt_u32 s55, 30
	s_cselect_b32 s0, 0, 0xffffffe0
	s_cselect_b32 s1, s18, s16
	s_add_i32 s0, s0, s28
	s_lshl_b32 s0, s0, 6
	s_add_i32 s0, s0, s1
	s_sub_i32 s0, s0, 64
	s_mul_i32 s64, s0, 0x1800
	s_add_u32 s66, s8, s96
	s_addc_u32 s67, s9, 0
	s_add_u32 s66, s66, s64
	s_addc_u32 s67, s67, 0
	s_add_u32 s68, s66, 0x30000
	s_addc_u32 s69, s67, 0
	s_add_u32 s70, s6, s96
	s_addc_u32 s71, s7, 0
	s_add_u32 s70, s70, s64
	s_addc_u32 s71, s71, 0
	s_add_u32 s72, s70, 0x30000
	s_addc_u32 s73, s71, 0
	global_load_dwordx4 v[146:149], v241, s[66:67]
	global_load_dwordx4 v[150:153], v241, s[68:69]
	global_load_dwordx4 v[154:157], v241, s[70:71]
	global_load_dwordx4 v[158:161], v241, s[72:73]
	s_lshl_b32 s20, s29, 14
	v_add_u32_e32 v180, s20, v194
	ds_read_b64_tr_b16 v[198:199], v180 offset:0
	ds_read_b64_tr_b16 v[200:201], v180 offset:0x800
	ds_read_b64_tr_b16 v[202:203], v180 offset:0x1000
	ds_read_b64_tr_b16 v[204:205], v180 offset:0x1800
	ds_read_b64_tr_b16 v[206:207], v180 offset:0x2000
	ds_read_b64_tr_b16 v[208:209], v180 offset:0x2800
	ds_read_b64_tr_b16 v[222:223], v180 offset:0x3000
	ds_read_b64_tr_b16 v[224:225], v180 offset:0x3800
	s_waitcnt lgkmcnt(0)
	s_nop 0
	v_mfma_f32_32x32x16_bf16 v[0:15], v[64:67], v[198:201], v[0:15]
	ds_read_b64_tr_b16 v[198:199], v180 offset:0x200
	ds_read_b64_tr_b16 v[200:201], v180 offset:0xa00
	v_mfma_f32_32x32x16_bf16 v[0:15], v[68:71], v[202:205], v[0:15]
	ds_read_b64_tr_b16 v[202:203], v180 offset:0x1200
	ds_read_b64_tr_b16 v[204:205], v180 offset:0x1a00
	v_mfma_f32_32x32x16_bf16 v[0:15], v[72:75], v[206:209], v[0:15]
	ds_read_b64_tr_b16 v[206:207], v180 offset:0x2200
	ds_read_b64_tr_b16 v[208:209], v180 offset:0x2a00
	v_mfma_f32_32x32x16_bf16 v[0:15], v[76:79], v[222:225], v[0:15]
	ds_read_b64_tr_b16 v[222:223], v180 offset:0x3200
	ds_read_b64_tr_b16 v[224:225], v180 offset:0x3a00
	s_waitcnt lgkmcnt(0)
	v_mfma_f32_32x32x16_bf16 v[48:63], v[64:67], v[198:201], v[48:63]
	ds_read_b64_tr_b16 v[198:199], v180 offset:0x400
	ds_read_b64_tr_b16 v[200:201], v180 offset:0xc00
	v_mfma_f32_32x32x16_bf16 v[48:63], v[68:71], v[202:205], v[48:63]
	ds_read_b64_tr_b16 v[202:203], v180 offset:0x1400
	ds_read_b64_tr_b16 v[204:205], v180 offset:0x1c00
	v_mfma_f32_32x32x16_bf16 v[48:63], v[72:75], v[206:209], v[48:63]
	ds_read_b64_tr_b16 v[206:207], v180 offset:0x2400
	ds_read_b64_tr_b16 v[208:209], v180 offset:0x2c00
	v_mfma_f32_32x32x16_bf16 v[48:63], v[76:79], v[222:225], v[48:63]
	ds_read_b64_tr_b16 v[222:223], v180 offset:0x3400
	ds_read_b64_tr_b16 v[224:225], v180 offset:0x3c00
	s_waitcnt lgkmcnt(0)
	v_mfma_f32_32x32x16_bf16 v[32:47], v[64:67], v[198:201], v[32:47]
	ds_read_b64_tr_b16 v[198:199], v180 offset:0x600
	ds_read_b64_tr_b16 v[200:201], v180 offset:0xe00
	v_mfma_f32_32x32x16_bf16 v[32:47], v[68:71], v[202:205], v[32:47]
	ds_read_b64_tr_b16 v[202:203], v180 offset:0x1600
	ds_read_b64_tr_b16 v[204:205], v180 offset:0x1e00
	v_mfma_f32_32x32x16_bf16 v[32:47], v[72:75], v[206:209], v[32:47]
	ds_read_b64_tr_b16 v[206:207], v180 offset:0x2600
	ds_read_b64_tr_b16 v[208:209], v180 offset:0x2e00
	v_mfma_f32_32x32x16_bf16 v[32:47], v[76:79], v[222:225], v[32:47]
	ds_read_b64_tr_b16 v[222:223], v180 offset:0x3600
	ds_read_b64_tr_b16 v[224:225], v180 offset:0x3e00
	s_waitcnt lgkmcnt(0)
	v_mfma_f32_32x32x16_bf16 v[16:31], v[64:67], v[198:201], v[16:31]
	v_max_f32_e32 v64, v96, v97
	v_max3_f32 v65, v80, v81, v82
	v_max3_f32 v64, v64, v98, v99
	v_max3_f32 v65, v65, v83, v84
	v_max3_f32 v64, v64, v100, v101
	v_mfma_f32_32x32x16_bf16 v[16:31], v[68:71], v[202:205], v[16:31]
	v_max3_f32 v65, v65, v85, v86
	v_max3_f32 v64, v64, v102, v103
	v_max3_f32 v65, v65, v87, v88
	v_max3_f32 v64, v64, v104, v105
	v_max3_f32 v65, v65, v89, v90
	v_max3_f32 v64, v64, v106, v107
	v_max3_f32 v65, v65, v91, v92
	v_mfma_f32_32x32x16_bf16 v[16:31], v[72:75], v[206:209], v[16:31]
	v_max3_f32 v64, v64, v108, v109
	v_max3_f32 v65, v65, v93, v94
	v_max3_f32 v64, v64, v110, v111
	v_max3_f32 v64, v64, v65, v95
	v_mov_b32_e32 v198, 1.0
	v_mfma_f32_32x32x16_bf16 v[16:31], v[76:79], v[222:225], v[16:31]
	v_cmp_ge_f32_e64 s[40:41], s75, v64
	s_and_b64 s[0:1], s[56:57], s[40:41]
	s_cmp_eq_u64 s[0:1], exec
	s_cbranch_scc0 .LBB0_801

.LBB0_792:
	v_exp_f32_e32 v197, v96
	v_exp_f32_e32 v208, v97
	v_exp_f32_e32 v209, v98
	v_exp_f32_e32 v210, v99
	v_exp_f32_e32 v211, v100
	v_exp_f32_e32 v220, v101
	v_exp_f32_e32 v221, v102
	v_exp_f32_e32 v222, v103
	v_exp_f32_e32 v223, v104
	v_exp_f32_e32 v224, v105
	v_exp_f32_e32 v225, v106
	v_exp_f32_e32 v226, v107
	v_exp_f32_e32 v227, v108
	v_exp_f32_e32 v228, v109
	v_exp_f32_e32 v229, v110
	v_exp_f32_e32 v230, v111
	s_waitcnt lgkmcnt(0)
	s_barrier
	v_add_u32_e32 v199, s22, v189
	v_add_u32_e32 v68, v199, v190
	ds_read_b128 v[64:67], v68 offset:50176
	ds_read_b128 v[68:71], v68 offset:58368
	v_add_u32_e32 v204, v199, v188
	ds_read_b128 v[200:203], v204 offset:50176
	ds_read_b128 v[204:207], v204 offset:58368
	v_exp_f32_e32 v231, v87
	s_waitcnt lgkmcnt(3)
	v_mfma_f32_32x32x16_bf16 v[96:111], v[64:67], v[122:125], 0
	v_exp_f32_e32 v232, v88
	v_exp_f32_e32 v233, v89
	v_exp_f32_e32 v234, v90
	v_exp_f32_e32 v235, v91
	v_exp_f32_e32 v236, v92
	v_exp_f32_e32 v237, v93
	v_exp_f32_e32 v238, v94
	s_waitcnt lgkmcnt(2)
	v_mfma_f32_32x32x16_bf16 v[64:79], v[68:71], v[122:125], 0
	v_exp_f32_e32 v95, v95
	s_waitcnt lgkmcnt(1)
	v_mfma_f32_32x32x16_bf16 v[96:111], v[200:203], v[126:129], v[96:111]
	s_waitcnt lgkmcnt(0)
	v_mfma_f32_32x32x16_bf16 v[64:79], v[204:207], v[126:129], v[64:79]
	v_add_u32_e32 v204, v199, v187
	ds_read_b128 v[200:203], v204 offset:50176
	ds_read_b128 v[204:207], v204 offset:58368
	v_add_u32_e32 v199, v199, v186
	s_waitcnt lgkmcnt(1)
	v_mfma_f32_32x32x16_bf16 v[96:111], v[200:203], v[118:121], v[96:111]
	s_waitcnt lgkmcnt(0)
	v_mfma_f32_32x32x16_bf16 v[64:79], v[204:207], v[118:121], v[64:79]
	ds_read_b128 v[200:203], v199 offset:50176
	ds_read_b128 v[204:207], v199 offset:58368
	s_waitcnt lgkmcnt(1)
	v_mfma_f32_32x32x16_bf16 v[96:111], v[200:203], v[114:117], v[96:111]
	v_exp_f32_e32 v201, v80
	v_add_f32_e32 v80, v208, v197
	v_add_f32_e32 v199, v209, v210
	v_add_f32_e32 v80, v211, v80
	v_add_f32_e32 v199, v220, v199
	v_add_f32_e32 v80, v221, v80
	v_add_f32_e32 v199, v222, v199
	v_add_f32_e32 v80, v223, v80
	v_add_f32_e32 v199, v224, v199
	v_add_f32_e32 v80, v225, v80
	v_add_f32_e32 v199, v226, v199
	v_add_f32_e32 v80, v227, v80
	v_exp_f32_e32 v202, v81
	v_add_f32_e32 v199, v228, v199
	v_exp_f32_e32 v203, v82
	v_add_f32_e32 v80, v229, v80
	s_waitcnt lgkmcnt(0)
	v_mfma_f32_32x32x16_bf16 v[64:79], v[204:207], v[114:117], v[64:79]
	v_exp_f32_e32 v204, v83
	v_add_f32_e32 v199, v230, v199
	v_exp_f32_e32 v205, v84
	v_add_f32_e32 v80, v201, v80
	v_exp_f32_e32 v206, v85
	v_add_f32_e32 v199, v202, v199
	v_exp_f32_e32 v207, v86
	v_add_f32_e32 v80, v203, v80
	v_add_f32_e32 v199, v204, v199
	v_add_f32_e32 v80, v205, v80
	v_add_f32_e32 v199, v206, v199
	v_add_f32_e32 v80, v207, v80
	v_add_f32_e32 v199, v231, v199
	v_add_f32_e32 v80, v232, v80
	v_add_f32_e32 v199, v233, v199
	v_add_f32_e32 v80, v234, v80
	v_add_f32_e32 v199, v235, v199
	v_add_f32_e32 v80, v236, v80
	v_add_f32_e32 v199, v237, v199
	v_add_f32_e32 v80, v238, v80
	v_add_f32_e32 v199, v95, v199
	v_add_f32_e32 v199, v199, v80
	v_cvt_pk_bf16_f32 v80, v197, v208
	v_cvt_pk_bf16_f32 v81, v209, v210
	v_cvt_pk_bf16_f32 v82, v211, v220
	v_cvt_pk_bf16_f32 v83, v221, v222
	v_cvt_pk_bf16_f32 v84, v223, v224
	v_cvt_pk_bf16_f32 v85, v225, v226
	v_cvt_pk_bf16_f32 v86, v227, v228
	v_cvt_pk_bf16_f32 v87, v229, v230
	v_cvt_pk_bf16_f32 v88, v201, v202
	v_cvt_pk_bf16_f32 v89, v203, v204
	v_cvt_pk_bf16_f32 v90, v205, v206
	v_cvt_pk_bf16_f32 v91, v207, v231
	v_cvt_pk_bf16_f32 v92, v232, v233
	v_cvt_pk_bf16_f32 v93, v234, v235
	v_cvt_pk_bf16_f32 v94, v236, v237
	v_cvt_pk_bf16_f32 v95, v238, v95
	s_cmp_gt_u32 s55, 32
	s_cbranch_scc1 .LBB0_794
	s_cmp_lt_u32 s55, 29
	s_cselect_b32 s0, 0, 0xffffffe0
	s_cselect_b32 s1, s18, s16
	s_add_i32 s0, s0, s28
	s_lshl_b32 s0, s0, 6
	s_add_i32 s0, s0, s1
	s_mul_i32 s64, s0, 0x1800
	s_add_u32 s66, s8, s96
	s_addc_u32 s67, s9, 0
	s_add_u32 s66, s66, s64
	s_addc_u32 s67, s67, 0
	s_add_u32 s68, s66, 0x30000
	s_addc_u32 s69, s67, 0
	s_add_u32 s70, s6, s96
	s_addc_u32 s71, s7, 0
	s_add_u32 s70, s70, s64
	s_addc_u32 s71, s71, 0
	s_add_u32 s72, s70, 0x30000
	s_addc_u32 s73, s71, 0
	global_load_dwordx4 v[130:133], v241, s[66:67]
	global_load_dwordx4 v[134:137], v241, s[68:69]
	global_load_dwordx4 v[138:141], v241, s[70:71]
	global_load_dwordx4 v[142:145], v241, s[72:73]
.LBB0_794:
	v_add_u32_e32 v197, s21, v194
	ds_read_b64_tr_b16 v[202:203], v197 offset:0
	ds_read_b64_tr_b16 v[204:205], v197 offset:0x800
	ds_read_b64_tr_b16 v[206:207], v197 offset:0x1000
	ds_read_b64_tr_b16 v[208:209], v197 offset:0x1800
	ds_read_b64_tr_b16 v[222:223], v197 offset:0x2000
	ds_read_b64_tr_b16 v[224:225], v197 offset:0x2800
	ds_read_b64_tr_b16 v[226:227], v197 offset:0x3000
	ds_read_b64_tr_b16 v[228:229], v197 offset:0x3800
	s_waitcnt lgkmcnt(0)
	s_nop 0
	v_mfma_f32_32x32x16_bf16 v[0:15], v[80:83], v[202:205], v[0:15]
	ds_read_b64_tr_b16 v[202:203], v197 offset:0x200
	ds_read_b64_tr_b16 v[204:205], v197 offset:0xa00
	v_mfma_f32_32x32x16_bf16 v[0:15], v[84:87], v[206:209], v[0:15]
	ds_read_b64_tr_b16 v[206:207], v197 offset:0x1200
	ds_read_b64_tr_b16 v[208:209], v197 offset:0x1a00
	v_mfma_f32_32x32x16_bf16 v[0:15], v[88:91], v[222:225], v[0:15]
	ds_read_b64_tr_b16 v[222:223], v197 offset:0x2200
	ds_read_b64_tr_b16 v[224:225], v197 offset:0x2a00
	v_mfma_f32_32x32x16_bf16 v[0:15], v[92:95], v[226:229], v[0:15]
	ds_read_b64_tr_b16 v[226:227], v197 offset:0x3200
	ds_read_b64_tr_b16 v[228:229], v197 offset:0x3a00
	s_waitcnt lgkmcnt(0)
	v_mfma_f32_32x32x16_bf16 v[48:63], v[80:83], v[202:205], v[48:63]
	ds_read_b64_tr_b16 v[202:203], v197 offset:0x400
	ds_read_b64_tr_b16 v[204:205], v197 offset:0xc00
	v_mfma_f32_32x32x16_bf16 v[48:63], v[84:87], v[206:209], v[48:63]
	ds_read_b64_tr_b16 v[206:207], v197 offset:0x1400
	ds_read_b64_tr_b16 v[208:209], v197 offset:0x1c00
	v_mfma_f32_32x32x16_bf16 v[48:63], v[88:91], v[222:225], v[48:63]
	ds_read_b64_tr_b16 v[222:223], v197 offset:0x2400
	ds_read_b64_tr_b16 v[224:225], v197 offset:0x2c00
	v_mfma_f32_32x32x16_bf16 v[48:63], v[92:95], v[226:229], v[48:63]
	ds_read_b64_tr_b16 v[226:227], v197 offset:0x3400
	ds_read_b64_tr_b16 v[228:229], v197 offset:0x3c00
	s_waitcnt lgkmcnt(0)
	v_mfma_f32_32x32x16_bf16 v[32:47], v[80:83], v[202:205], v[32:47]
	ds_read_b64_tr_b16 v[202:203], v197 offset:0x600
	ds_read_b64_tr_b16 v[204:205], v197 offset:0xe00
	v_mfma_f32_32x32x16_bf16 v[32:47], v[84:87], v[206:209], v[32:47]
	ds_read_b64_tr_b16 v[206:207], v197 offset:0x1600
	ds_read_b64_tr_b16 v[208:209], v197 offset:0x1e00
	v_mfma_f32_32x32x16_bf16 v[32:47], v[88:91], v[222:225], v[32:47]
	ds_read_b64_tr_b16 v[222:223], v197 offset:0x2600
	ds_read_b64_tr_b16 v[224:225], v197 offset:0x2e00
	v_mfma_f32_32x32x16_bf16 v[32:47], v[92:95], v[226:229], v[32:47]
	ds_read_b64_tr_b16 v[226:227], v197 offset:0x3600
	ds_read_b64_tr_b16 v[228:229], v197 offset:0x3e00
	s_waitcnt lgkmcnt(0)
	v_mfma_f32_32x32x16_bf16 v[16:31], v[80:83], v[202:205], v[16:31]
	v_max_f32_e32 v80, v96, v97
	v_max3_f32 v81, v64, v65, v66
	v_max3_f32 v80, v80, v98, v99
	v_max3_f32 v81, v81, v67, v68
	v_max3_f32 v80, v80, v100, v101
	v_mfma_f32_32x32x16_bf16 v[16:31], v[84:87], v[206:209], v[16:31]
	v_max3_f32 v81, v81, v69, v70
	v_max3_f32 v80, v80, v102, v103
	v_max3_f32 v81, v81, v71, v72
	v_max3_f32 v80, v80, v104, v105
	v_max3_f32 v81, v81, v73, v74
	v_max3_f32 v80, v80, v106, v107
	v_max3_f32 v81, v81, v75, v76
	v_mfma_f32_32x32x16_bf16 v[16:31], v[88:91], v[222:225], v[16:31]
	v_max3_f32 v80, v80, v108, v109
	v_max3_f32 v81, v81, v77, v78
	v_max3_f32 v80, v80, v110, v111
	v_max3_f32 v80, v80, v81, v79
	v_mov_b32_e32 v197, 1.0
	v_mfma_f32_32x32x16_bf16 v[16:31], v[92:95], v[226:229], v[16:31]
	v_cmp_ge_f32_e64 s[40:41], s75, v80
	s_and_b64 s[0:1], s[56:57], s[40:41]
	s_cmp_eq_u64 s[0:1], exec
	s_cbranch_scc0 .LBB0_802

.LBB0_799:
	v_exp_f32_e32 v159, v96
	v_exp_f32_e32 v161, v97
	v_exp_f32_e32 v157, v98
	v_exp_f32_e32 v160, v99
	v_exp_f32_e32 v155, v100
	v_exp_f32_e32 v158, v101
	v_exp_f32_e32 v154, v102
	v_exp_f32_e32 v156, v103
	v_exp_f32_e32 v151, v104
	v_exp_f32_e32 v153, v105
	v_exp_f32_e32 v149, v106
	v_exp_f32_e32 v152, v107
	v_exp_f32_e32 v147, v108
	v_exp_f32_e32 v150, v109
	v_exp_f32_e32 v146, v110
	v_exp_f32_e32 v148, v111
	v_fma_f32 v80, v193, v179, v195
	s_add_i32 s28, s28, 2
	v_fma_f32 v179, v80, v198, v199
	s_cmp_gt_u32 s55, 32
	s_waitcnt lgkmcnt(0)
	s_barrier
	s_cbranch_scc1 .LBB0_803
	s_mov_b32 s0, s29
	s_mov_b32 s29, s19
	s_mov_b32 s19, s54
	v_mov_b32_e32 v193, v197
	s_branch .LBB0_787
.LBB0_801:
	v_mov_b32_e32 v65, v64
	s_nop 1
	v_permlane32_swap_b32_e32 v64, v65
	v_max_f32_e32 v64, v64, v65
	v_sub_f32_e32 v65, v64, v164
	v_cmp_lt_f32_e32 vcc, s75, v65
	v_max_f32_e32 v64, v64, v64
	v_max_f32_e32 v65, v164, v164
	v_max_f32_e32 v64, v65, v64
	v_cndmask_b32_e32 v64, v164, v64, vcc
	v_sub_f32_e32 v65, v164, v64
	v_exp_f32_e32 v198, v65
	v_pk_add_f32 v[96:97], v[96:97], v[64:65] op_sel_hi:[1,0] neg_lo:[0,1] neg_hi:[0,1]
	v_pk_add_f32 v[98:99], v[98:99], v[64:65] op_sel_hi:[1,0] neg_lo:[0,1] neg_hi:[0,1]
	v_pk_add_f32 v[100:101], v[100:101], v[64:65] op_sel_hi:[1,0] neg_lo:[0,1] neg_hi:[0,1]
	v_pk_add_f32 v[102:103], v[102:103], v[64:65] op_sel_hi:[1,0] neg_lo:[0,1] neg_hi:[0,1]
	v_pk_add_f32 v[104:105], v[104:105], v[64:65] op_sel_hi:[1,0] neg_lo:[0,1] neg_hi:[0,1]
	v_pk_add_f32 v[106:107], v[106:107], v[64:65] op_sel_hi:[1,0] neg_lo:[0,1] neg_hi:[0,1]
	v_pk_add_f32 v[108:109], v[108:109], v[64:65] op_sel_hi:[1,0] neg_lo:[0,1] neg_hi:[0,1]
	v_pk_add_f32 v[110:111], v[110:111], v[64:65] op_sel_hi:[1,0] neg_lo:[0,1] neg_hi:[0,1]
	v_sub_f32_e32 v95, v95, v64
	v_sub_f32_e32 v94, v94, v64
	v_sub_f32_e32 v93, v93, v64
	v_sub_f32_e32 v92, v92, v64
	v_sub_f32_e32 v91, v91, v64
	v_sub_f32_e32 v90, v90, v64
	v_sub_f32_e32 v89, v89, v64
	v_sub_f32_e32 v88, v88, v64
	v_sub_f32_e32 v87, v87, v64
	v_sub_f32_e32 v86, v86, v64
	v_sub_f32_e32 v85, v85, v64
	v_sub_f32_e32 v84, v84, v64
	v_sub_f32_e32 v83, v83, v64
	v_sub_f32_e32 v82, v82, v64
	v_sub_f32_e32 v81, v81, v64
	v_sub_f32_e32 v80, v80, v64
	v_mov_b32_e32 v164, v64
	v_cmp_eq_f32_e64 s[56:57], 0, v164
	s_branch .LBB0_788
.LBB0_802:
	v_mov_b32_e32 v81, v80
	s_nop 1
	v_permlane32_swap_b32_e32 v80, v81
	v_max_f32_e32 v80, v80, v81
	v_sub_f32_e32 v81, v80, v164
	v_cmp_lt_f32_e32 vcc, s75, v81
	v_max_f32_e32 v80, v80, v80
	v_max_f32_e32 v81, v164, v164
	v_max_f32_e32 v80, v81, v80
	v_cndmask_b32_e32 v80, v164, v80, vcc
	v_sub_f32_e32 v81, v164, v80
	v_exp_f32_e32 v197, v81
	v_pk_add_f32 v[96:97], v[96:97], v[80:81] op_sel_hi:[1,0] neg_lo:[0,1] neg_hi:[0,1]
	v_pk_add_f32 v[98:99], v[98:99], v[80:81] op_sel_hi:[1,0] neg_lo:[0,1] neg_hi:[0,1]
	v_pk_add_f32 v[100:101], v[100:101], v[80:81] op_sel_hi:[1,0] neg_lo:[0,1] neg_hi:[0,1]
	v_pk_add_f32 v[102:103], v[102:103], v[80:81] op_sel_hi:[1,0] neg_lo:[0,1] neg_hi:[0,1]
	v_pk_add_f32 v[104:105], v[104:105], v[80:81] op_sel_hi:[1,0] neg_lo:[0,1] neg_hi:[0,1]
	v_pk_add_f32 v[106:107], v[106:107], v[80:81] op_sel_hi:[1,0] neg_lo:[0,1] neg_hi:[0,1]
	v_pk_add_f32 v[108:109], v[108:109], v[80:81] op_sel_hi:[1,0] neg_lo:[0,1] neg_hi:[0,1]
	v_pk_add_f32 v[110:111], v[110:111], v[80:81] op_sel_hi:[1,0] neg_lo:[0,1] neg_hi:[0,1]
	v_sub_f32_e32 v79, v79, v80
	v_sub_f32_e32 v78, v78, v80
	v_sub_f32_e32 v77, v77, v80
	v_sub_f32_e32 v76, v76, v80
	v_sub_f32_e32 v75, v75, v80
	v_sub_f32_e32 v74, v74, v80
	v_sub_f32_e32 v73, v73, v80
	v_sub_f32_e32 v72, v72, v80
	v_sub_f32_e32 v71, v71, v80
	v_sub_f32_e32 v70, v70, v80
	v_sub_f32_e32 v69, v69, v80
	v_sub_f32_e32 v68, v68, v80
	v_sub_f32_e32 v67, v67, v80
	v_sub_f32_e32 v66, v66, v80
	v_sub_f32_e32 v65, v65, v80
	v_sub_f32_e32 v64, v64, v80
	v_mov_b32_e32 v164, v80
	v_cmp_eq_f32_e64 s[56:57], 0, v164
	s_branch .LBB0_795
.LBB0_803:
	v_add_u32_e32 v134, s20, v189
	v_add_u32_e32 v84, v134, v190
	ds_read_b128 v[80:83], v84 offset:50176
	ds_read_b128 v[84:87], v84 offset:58368
	v_add_u32_e32 v130, v134, v188
	v_exp_f32_e32 v78, v78
	v_exp_f32_e32 v79, v79
	s_waitcnt lgkmcnt(1)
	v_mfma_f32_32x32x16_bf16 v[96:111], v[80:83], v[122:125], 0
	s_waitcnt lgkmcnt(0)
	v_mfma_f32_32x32x16_bf16 v[80:95], v[84:87], v[122:125], 0
	ds_read_b128 v[122:125], v130 offset:50176
	ds_read_b128 v[130:133], v130 offset:58368
	s_waitcnt lgkmcnt(1)
	v_mfma_f32_32x32x16_bf16 v[96:111], v[122:125], v[126:129], v[96:111]
	s_waitcnt lgkmcnt(0)
	v_mfma_f32_32x32x16_bf16 v[80:95], v[130:133], v[126:129], v[80:95]
	v_add_u32_e32 v126, v134, v187
	ds_read_b128 v[122:125], v126 offset:50176
	ds_read_b128 v[126:129], v126 offset:58368
	s_waitcnt lgkmcnt(1)
	v_mfma_f32_32x32x16_bf16 v[96:111], v[122:125], v[118:121], v[96:111]
	v_add_u32_e32 v122, v134, v186
	s_waitcnt lgkmcnt(0)
	v_mfma_f32_32x32x16_bf16 v[80:95], v[126:129], v[118:121], v[80:95]
	ds_read_b128 v[118:121], v122 offset:50176
	ds_read_b128 v[122:125], v122 offset:58368
	v_exp_f32_e32 v126, v76
	v_exp_f32_e32 v127, v77
	s_waitcnt lgkmcnt(1)
	v_mfma_f32_32x32x16_bf16 v[96:111], v[118:121], v[114:117], v[96:111]
	v_exp_f32_e32 v118, v68
	v_exp_f32_e32 v119, v69
	v_exp_f32_e32 v120, v70
	v_exp_f32_e32 v121, v71
	s_waitcnt lgkmcnt(0)
	v_mfma_f32_32x32x16_bf16 v[80:95], v[122:125], v[114:117], v[80:95]
	v_exp_f32_e32 v114, v64
	v_add_f32_e32 v64, 0, v159
	v_add_f32_e32 v64, v161, v64
	v_add_f32_e32 v64, v157, v64
	v_add_f32_e32 v64, v160, v64
	v_add_f32_e32 v64, v155, v64
	v_add_f32_e32 v64, v158, v64
	v_add_f32_e32 v64, v154, v64
	v_add_f32_e32 v64, v156, v64
	v_add_f32_e32 v64, v151, v64
	v_add_f32_e32 v64, v153, v64
	v_add_f32_e32 v64, v149, v64
	v_add_f32_e32 v64, v152, v64
	v_add_f32_e32 v64, v147, v64
	v_exp_f32_e32 v115, v65
	v_add_f32_e32 v64, v150, v64
	v_exp_f32_e32 v116, v66
	v_add_f32_e32 v64, v146, v64
	v_exp_f32_e32 v117, v67
	v_add_f32_e32 v64, v148, v64
	v_add_f32_e32 v64, v114, v64
	v_add_f32_e32 v64, v115, v64
	v_add_f32_e32 v64, v116, v64
	v_add_f32_e32 v64, v117, v64
	v_exp_f32_e32 v122, v72
	v_add_f32_e32 v64, v118, v64
	v_exp_f32_e32 v123, v73
	v_add_f32_e32 v64, v119, v64
	v_exp_f32_e32 v124, v74
	v_add_f32_e32 v64, v120, v64
	v_exp_f32_e32 v125, v75
	v_add_f32_e32 v64, v121, v64
	v_add_f32_e32 v64, v122, v64
	v_add_f32_e32 v64, v123, v64
	v_add_f32_e32 v64, v124, v64
	v_add_f32_e32 v64, v125, v64
	v_add_f32_e32 v64, v126, v64
	v_add_f32_e32 v64, v127, v64
	v_add_f32_e32 v64, v78, v64
	v_add_f32_e32 v64, v79, v64
	v_cvt_pk_bf16_f32 v66, v159, v161
	v_cvt_pk_bf16_f32 v67, v157, v160
	v_cvt_pk_bf16_f32 v68, v155, v158
	v_cvt_pk_bf16_f32 v69, v154, v156
	v_cvt_pk_bf16_f32 v70, v151, v153
	v_cvt_pk_bf16_f32 v71, v149, v152
	v_cvt_pk_bf16_f32 v72, v147, v150
	v_cvt_pk_bf16_f32 v73, v146, v148
	v_cvt_pk_bf16_f32 v74, v114, v115
	v_cvt_pk_bf16_f32 v75, v116, v117
	v_cvt_pk_bf16_f32 v76, v118, v119
	v_cvt_pk_bf16_f32 v77, v120, v121
	v_cvt_pk_bf16_f32 v114, v122, v123
	v_cvt_pk_bf16_f32 v115, v124, v125
	v_cvt_pk_bf16_f32 v116, v126, v127
	v_cvt_pk_bf16_f32 v117, v78, v79
	s_nop 0
	s_add_i32 s0, 0, 0x4400
	v_add_u32_e32 v78, s0, v192
	ds_read_b64_tr_b16 v[118:119], v78 offset:0
	ds_read_b64_tr_b16 v[120:121], v78 offset:0x800
	ds_read_b64_tr_b16 v[122:123], v78 offset:0x1000
	ds_read_b64_tr_b16 v[124:125], v78 offset:0x1800
	ds_read_b64_tr_b16 v[126:127], v78 offset:0x2000
	ds_read_b64_tr_b16 v[128:129], v78 offset:0x2800
	ds_read_b64_tr_b16 v[130:131], v78 offset:0x3000
	ds_read_b64_tr_b16 v[132:133], v78 offset:0x3800
	s_waitcnt lgkmcnt(0)
	s_nop 0
	v_mfma_f32_32x32x16_bf16 v[0:15], v[66:69], v[118:121], v[0:15]
	ds_read_b64_tr_b16 v[118:119], v78 offset:0x200
	ds_read_b64_tr_b16 v[120:121], v78 offset:0xa00
	v_mfma_f32_32x32x16_bf16 v[0:15], v[70:73], v[122:125], v[0:15]
	ds_read_b64_tr_b16 v[122:123], v78 offset:0x1200
	ds_read_b64_tr_b16 v[124:125], v78 offset:0x1a00
	v_mfma_f32_32x32x16_bf16 v[0:15], v[74:77], v[126:129], v[0:15]
	ds_read_b64_tr_b16 v[126:127], v78 offset:0x2200
	ds_read_b64_tr_b16 v[128:129], v78 offset:0x2a00
	v_mfma_f32_32x32x16_bf16 v[0:15], v[114:117], v[130:133], v[0:15]
	ds_read_b64_tr_b16 v[130:131], v78 offset:0x3200
	ds_read_b64_tr_b16 v[132:133], v78 offset:0x3a00
	s_waitcnt lgkmcnt(0)
	v_mfma_f32_32x32x16_bf16 v[48:63], v[66:69], v[118:121], v[48:63]
	ds_read_b64_tr_b16 v[118:119], v78 offset:0x400
	ds_read_b64_tr_b16 v[120:121], v78 offset:0xc00
	v_mfma_f32_32x32x16_bf16 v[48:63], v[70:73], v[122:125], v[48:63]
	ds_read_b64_tr_b16 v[122:123], v78 offset:0x1400
	ds_read_b64_tr_b16 v[124:125], v78 offset:0x1c00
	v_mfma_f32_32x32x16_bf16 v[48:63], v[74:77], v[126:129], v[48:63]
	ds_read_b64_tr_b16 v[126:127], v78 offset:0x2400
	ds_read_b64_tr_b16 v[128:129], v78 offset:0x2c00
	v_mfma_f32_32x32x16_bf16 v[48:63], v[114:117], v[130:133], v[48:63]
	ds_read_b64_tr_b16 v[130:131], v78 offset:0x3400
	ds_read_b64_tr_b16 v[132:133], v78 offset:0x3c00
	s_waitcnt lgkmcnt(0)
	v_mfma_f32_32x32x16_bf16 v[32:47], v[66:69], v[118:121], v[32:47]
	ds_read_b64_tr_b16 v[118:119], v78 offset:0x600
	ds_read_b64_tr_b16 v[120:121], v78 offset:0xe00
	v_mfma_f32_32x32x16_bf16 v[32:47], v[70:73], v[122:125], v[32:47]
	ds_read_b64_tr_b16 v[122:123], v78 offset:0x1600
	ds_read_b64_tr_b16 v[124:125], v78 offset:0x1e00
	v_mfma_f32_32x32x16_bf16 v[32:47], v[74:77], v[126:129], v[32:47]
	ds_read_b64_tr_b16 v[126:127], v78 offset:0x2600
	ds_read_b64_tr_b16 v[128:129], v78 offset:0x2e00
	v_mfma_f32_32x32x16_bf16 v[32:47], v[114:117], v[130:133], v[32:47]
	ds_read_b64_tr_b16 v[130:131], v78 offset:0x3600
	ds_read_b64_tr_b16 v[132:133], v78 offset:0x3e00
	s_waitcnt lgkmcnt(0)
	v_mfma_f32_32x32x16_bf16 v[16:31], v[66:69], v[118:121], v[16:31]
	v_max_f32_e32 v66, v97, v97
	v_max_f32_e32 v67, v96, v96
	v_max_f32_e32 v66, v67, v66
	v_max3_f32 v66, v66, v98, v99
	v_max3_f32 v66, v66, v100, v101
	v_max3_f32 v66, v66, v102, v103
	v_max3_f32 v66, v66, v104, v105
	v_mfma_f32_32x32x16_bf16 v[16:31], v[70:73], v[122:125], v[16:31]
	v_max3_f32 v66, v66, v106, v107
	v_max3_f32 v66, v66, v108, v109
	v_max3_f32 v66, v66, v110, v111
	v_max3_f32 v66, v66, v80, v81
	v_max3_f32 v66, v66, v82, v83
	v_max3_f32 v66, v66, v84, v85
	v_max3_f32 v66, v66, v86, v87
	v_mfma_f32_32x32x16_bf16 v[16:31], v[74:77], v[126:129], v[16:31]
	v_max3_f32 v66, v66, v88, v89
	v_max3_f32 v66, v66, v90, v91
	v_max3_f32 v66, v66, v92, v93
	v_max3_f32 v66, v66, v94, v95
	v_mov_b32_e32 v67, v66
	s_nop 1
	v_permlane32_swap_b32_e32 v66, v67
	v_mfma_f32_32x32x16_bf16 v[16:31], v[114:117], v[130:133], v[16:31]
	v_max_f32_e32 v67, v67, v67
	v_max_f32_e32 v66, v66, v66
	v_max_f32_e32 v67, v66, v67
	v_cmp_eq_f32_e32 vcc, 0, v164
	v_cmp_ge_f32_e64 s[40:41], s75, v67
	s_and_b64 s[0:1], vcc, s[40:41]
	v_cndmask_b32_e64 v66, 0, 1, s[0:1]
	v_cmp_ne_u32_e32 vcc, 0, v66
	s_cmp_eq_u64 vcc, exec
	v_mov_b32_e32 v66, 1.0
	s_cbranch_scc0 .LBB0_815
	v_cmp_gt_f32_e32 vcc, 1.0, v66
	s_cbranch_vccz .LBB0_808

.LBB0_808:
	v_exp_f32_e32 v69, v96
	v_exp_f32_e32 v70, v97
	v_exp_f32_e32 v71, v98
	v_exp_f32_e32 v72, v99
	v_exp_f32_e32 v73, v100
	v_add_f32_e32 v67, 0, v69
	v_exp_f32_e32 v74, v101
	v_add_f32_e32 v67, v70, v67
	v_exp_f32_e32 v75, v102
	v_add_f32_e32 v67, v71, v67
	v_exp_f32_e32 v76, v103
	v_add_f32_e32 v67, v72, v67
	v_exp_f32_e32 v77, v104
	v_add_f32_e32 v67, v73, v67
	v_exp_f32_e32 v78, v105
	v_add_f32_e32 v67, v74, v67
	v_exp_f32_e32 v79, v106
	v_add_f32_e32 v67, v75, v67
	v_exp_f32_e32 v96, v107
	v_add_f32_e32 v67, v76, v67
	v_exp_f32_e32 v97, v108
	v_add_f32_e32 v67, v77, v67
	v_exp_f32_e32 v98, v109
	v_add_f32_e32 v67, v78, v67
	v_exp_f32_e32 v99, v110
	v_add_f32_e32 v67, v79, v67
	v_exp_f32_e32 v100, v111
	v_add_f32_e32 v67, v96, v67
	v_exp_f32_e32 v80, v80
	v_add_f32_e32 v67, v97, v67
	v_exp_f32_e32 v81, v81
	v_add_f32_e32 v67, v98, v67
	v_exp_f32_e32 v82, v82
	v_add_f32_e32 v67, v99, v67
	v_exp_f32_e32 v83, v83
	v_add_f32_e32 v67, v100, v67
	v_exp_f32_e32 v84, v84
	v_add_f32_e32 v67, v80, v67
	v_exp_f32_e32 v85, v85
	v_add_f32_e32 v67, v81, v67
	v_exp_f32_e32 v86, v86
	v_add_f32_e32 v67, v82, v67
	v_exp_f32_e32 v87, v87
	v_add_f32_e32 v67, v83, v67
	v_exp_f32_e32 v88, v88
	v_add_f32_e32 v67, v84, v67
	v_exp_f32_e32 v89, v89
	v_add_f32_e32 v67, v85, v67
	v_exp_f32_e32 v90, v90
	v_add_f32_e32 v67, v86, v67
	v_exp_f32_e32 v91, v91
	v_add_f32_e32 v67, v87, v67
	v_exp_f32_e32 v92, v92
	v_add_f32_e32 v67, v88, v67
	v_exp_f32_e32 v93, v93
	v_add_f32_e32 v67, v89, v67
	v_exp_f32_e32 v94, v94
	v_add_f32_e32 v67, v90, v67
	v_exp_f32_e32 v95, v95
	v_add_f32_e32 v67, v91, v67
	v_add_f32_e32 v67, v92, v67
	v_add_f32_e32 v67, v93, v67
	v_add_f32_e32 v67, v94, v67
	v_add_f32_e32 v67, v95, v67
	v_cvt_pk_bf16_f32 v70, v69, v70
	v_cvt_pk_bf16_f32 v71, v71, v72
	v_cvt_pk_bf16_f32 v72, v73, v74
	v_cvt_pk_bf16_f32 v73, v75, v76
	v_cvt_pk_bf16_f32 v74, v77, v78
	v_cvt_pk_bf16_f32 v75, v79, v96
	v_cvt_pk_bf16_f32 v76, v97, v98
	v_cvt_pk_bf16_f32 v77, v99, v100
	v_cvt_pk_bf16_f32 v78, v80, v81
	v_cvt_pk_bf16_f32 v79, v82, v83
	v_cvt_pk_bf16_f32 v80, v84, v85
	v_cvt_pk_bf16_f32 v81, v86, v87
	v_cvt_pk_bf16_f32 v82, v88, v89
	v_cvt_pk_bf16_f32 v83, v90, v91
	v_cvt_pk_bf16_f32 v84, v92, v93
	v_cvt_pk_bf16_f32 v85, v94, v95
	s_nop 0
	ds_read_b64_tr_b16 v[86:87], v180 offset:0
	ds_read_b64_tr_b16 v[88:89], v180 offset:0x800
	ds_read_b64_tr_b16 v[90:91], v180 offset:0x1000
	ds_read_b64_tr_b16 v[92:93], v180 offset:0x1800
	ds_read_b64_tr_b16 v[94:95], v180 offset:0x2000
	ds_read_b64_tr_b16 v[96:97], v180 offset:0x2800
	ds_read_b64_tr_b16 v[98:99], v180 offset:0x3000
	ds_read_b64_tr_b16 v[100:101], v180 offset:0x3800
	s_waitcnt lgkmcnt(0)
	s_nop 0
	v_mfma_f32_32x32x16_bf16 v[0:15], v[70:73], v[86:89], v[0:15]
	ds_read_b64_tr_b16 v[86:87], v180 offset:0x200
	ds_read_b64_tr_b16 v[88:89], v180 offset:0xa00
	v_mfma_f32_32x32x16_bf16 v[0:15], v[74:77], v[90:93], v[0:15]
	ds_read_b64_tr_b16 v[90:91], v180 offset:0x1200
	ds_read_b64_tr_b16 v[92:93], v180 offset:0x1a00
	v_mfma_f32_32x32x16_bf16 v[0:15], v[78:81], v[94:97], v[0:15]
	ds_read_b64_tr_b16 v[94:95], v180 offset:0x2200
	ds_read_b64_tr_b16 v[96:97], v180 offset:0x2a00
	v_mfma_f32_32x32x16_bf16 v[0:15], v[82:85], v[98:101], v[0:15]
	ds_read_b64_tr_b16 v[98:99], v180 offset:0x3200
	ds_read_b64_tr_b16 v[100:101], v180 offset:0x3a00
	s_waitcnt lgkmcnt(0)
	v_mfma_f32_32x32x16_bf16 v[48:63], v[70:73], v[86:89], v[48:63]
	ds_read_b64_tr_b16 v[86:87], v180 offset:0x400
	ds_read_b64_tr_b16 v[88:89], v180 offset:0xc00
	v_mfma_f32_32x32x16_bf16 v[48:63], v[74:77], v[90:93], v[48:63]
	ds_read_b64_tr_b16 v[90:91], v180 offset:0x1400
	ds_read_b64_tr_b16 v[92:93], v180 offset:0x1c00
	v_mfma_f32_32x32x16_bf16 v[48:63], v[78:81], v[94:97], v[48:63]
	ds_read_b64_tr_b16 v[94:95], v180 offset:0x2400
	ds_read_b64_tr_b16 v[96:97], v180 offset:0x2c00
	v_mfma_f32_32x32x16_bf16 v[48:63], v[82:85], v[98:101], v[48:63]
	ds_read_b64_tr_b16 v[98:99], v180 offset:0x3400
	ds_read_b64_tr_b16 v[100:101], v180 offset:0x3c00
	s_waitcnt lgkmcnt(0)
	v_mfma_f32_32x32x16_bf16 v[32:47], v[70:73], v[86:89], v[32:47]
	ds_read_b64_tr_b16 v[86:87], v180 offset:0x600
	ds_read_b64_tr_b16 v[88:89], v180 offset:0xe00
	v_mfma_f32_32x32x16_bf16 v[32:47], v[74:77], v[90:93], v[32:47]
	ds_read_b64_tr_b16 v[90:91], v180 offset:0x1600
	ds_read_b64_tr_b16 v[92:93], v180 offset:0x1e00
	v_mfma_f32_32x32x16_bf16 v[32:47], v[78:81], v[94:97], v[32:47]
	ds_read_b64_tr_b16 v[94:95], v180 offset:0x2600
	ds_read_b64_tr_b16 v[96:97], v180 offset:0x2e00
	v_mfma_f32_32x32x16_bf16 v[32:47], v[82:85], v[98:101], v[32:47]
	ds_read_b64_tr_b16 v[98:99], v180 offset:0x3600
	ds_read_b64_tr_b16 v[100:101], v180 offset:0x3e00
	s_waitcnt lgkmcnt(0)
	v_mfma_f32_32x32x16_bf16 v[16:31], v[70:73], v[86:89], v[16:31]
	v_mfma_f32_32x32x16_bf16 v[16:31], v[74:77], v[90:93], v[16:31]
	v_mfma_f32_32x32x16_bf16 v[16:31], v[78:81], v[94:97], v[16:31]
	v_mfma_f32_32x32x16_bf16 v[16:31], v[82:85], v[98:101], v[16:31]
	v_fma_f32 v64, v179, v197, v64
	v_fma_f32 v65, v64, v66, v67
	v_mov_b32_e32 v64, v65
	s_nop 1
	v_permlane32_swap_b32_e32 v65, v64
	v_add_f32_e32 v65, v65, v64
	s_and_saveexec_b64 s[0:1], s[38:39]
	s_cbranch_execz .LBB0_761
	ds_write_b32 v178, v65
	s_branch .LBB0_761

.LBB0_814:
	v_cmp_lt_f32_e32 vcc, s75, v34
	v_max_f32_e32 v34, v34, v34
	v_max_f32_e32 v34, 0, v34
	v_cndmask_b32_e32 v164, 0, v34, vcc
	v_cmp_eq_f32_e64 s[56:57], 0, v164
	v_exp_f32_e64 v193, -v164
	v_pk_add_f32 v[0:1], v[0:1], v[164:165] op_sel_hi:[1,0] neg_lo:[0,1] neg_hi:[0,1]
	v_pk_add_f32 v[2:3], v[2:3], v[164:165] op_sel_hi:[1,0] neg_lo:[0,1] neg_hi:[0,1]
	v_pk_add_f32 v[4:5], v[4:5], v[164:165] op_sel_hi:[1,0] neg_lo:[0,1] neg_hi:[0,1]
	v_pk_add_f32 v[6:7], v[6:7], v[164:165] op_sel_hi:[1,0] neg_lo:[0,1] neg_hi:[0,1]
	v_pk_add_f32 v[8:9], v[8:9], v[164:165] op_sel_hi:[1,0] neg_lo:[0,1] neg_hi:[0,1]
	v_pk_add_f32 v[10:11], v[10:11], v[164:165] op_sel_hi:[1,0] neg_lo:[0,1] neg_hi:[0,1]
	v_pk_add_f32 v[12:13], v[12:13], v[164:165] op_sel_hi:[1,0] neg_lo:[0,1] neg_hi:[0,1]
	v_pk_add_f32 v[14:15], v[14:15], v[164:165] op_sel_hi:[1,0] neg_lo:[0,1] neg_hi:[0,1]
	v_sub_f32_e32 v79, v79, v164
	v_sub_f32_e32 v78, v78, v164
	v_sub_f32_e32 v77, v77, v164
	v_sub_f32_e32 v76, v76, v164
	v_sub_f32_e32 v75, v75, v164
	v_sub_f32_e32 v74, v74, v164
	v_sub_f32_e32 v73, v73, v164
	v_sub_f32_e32 v72, v72, v164
	v_sub_f32_e32 v71, v71, v164
	v_sub_f32_e32 v70, v70, v164
	v_sub_f32_e32 v69, v69, v164
	v_sub_f32_e32 v68, v68, v164
	v_sub_f32_e32 v67, v67, v164
	v_sub_f32_e32 v66, v66, v164
	v_sub_f32_e32 v65, v65, v164
	v_sub_f32_e32 v64, v64, v164
	s_branch .LBB0_786
